# speedup vs baseline: 1.0071x; 1.0071x over previous
.LBB2_5:
	s_lshl_b32 s6, s26, 5
	s_and_b32 s6, s6, 0x700
	v_or_b32_e32 v200, s6, v213
	s_lshl_b32 s6, s24, 8
	s_sub_i32 s6, 0x400000, s6
	s_and_b32 s5, s5, 0xffff
	s_andn2_b64 vcc, exec, s[22:23]
	s_and_b32 s21, s19, 0xffff
	s_cbranch_vccnz .LBB2_7
	s_lshl_b64 s[16:17], s[16:17], 22
	s_add_u32 s16, s8, s16
	s_addc_u32 s17, s9, s17
	s_and_b32 s17, s17, 0xffff
	s_cmp_lg_u32 0, -1
	s_cselect_b32 s22, 0, 0
	s_add_i32 s22, s22, s81
	v_lshl_or_b32 v32, v200, 11, s35
	s_mov_b32 s19, s7
	s_add_i32 s23, s22, 0x10000
	v_readfirstlane_b32 s24, v32
	s_nop 4
	s_mov_b32 m0, s23
	s_nop 0
	buffer_load_dwordx4 v209, s[16:19], s24 offen lds
	s_add_i32 s23, s22, 0x10400
	s_or_b32 s81, s24, 0x2000
	s_nop 4
	s_mov_b32 m0, s23
	s_nop 0
	buffer_load_dwordx4 v210, s[16:19], s81 offen lds
	s_add_i32 s23, s22, 0x10800
	s_or_b32 s81, s24, 0x4000
	s_nop 4
	s_mov_b32 m0, s23
	s_nop 0
	buffer_load_dwordx4 v209, s[16:19], s81 offen lds
	s_add_i32 s23, s22, 0x10c00
	s_or_b32 s81, s24, 0x6000
	s_nop 4
	s_mov_b32 m0, s23
	s_nop 0
	buffer_load_dwordx4 v210, s[16:19], s81 offen lds
	s_add_i32 s23, s22, 0x11000
	s_or_b32 s81, s24, 0x8000
	s_nop 4
	s_mov_b32 m0, s23
	s_nop 0
	buffer_load_dwordx4 v209, s[16:19], s81 offen lds
	s_add_i32 s23, s22, 0x11400
	s_or_b32 s81, s24, 0xa000
	s_nop 4
	s_mov_b32 m0, s23
	s_nop 0
	buffer_load_dwordx4 v210, s[16:19], s81 offen lds
	s_add_i32 s23, s22, 0x11800
	s_or_b32 s81, s24, 0xc000
	s_nop 4
	s_mov_b32 m0, s23
	s_nop 0
	buffer_load_dwordx4 v209, s[16:19], s81 offen lds
	s_add_i32 s23, s22, 0x11c00
	s_or_b32 s81, s24, 0xe000
	s_nop 4
	s_mov_b32 m0, s23
	s_nop 0
	buffer_load_dwordx4 v210, s[16:19], s81 offen lds
	s_add_i32 s23, s22, 0x12000
	s_or_b32 s81, s24, 0x10000
	s_nop 4
	s_mov_b32 m0, s23
	s_nop 0
	buffer_load_dwordx4 v209, s[16:19], s81 offen lds
	s_add_i32 s23, s22, 0x12400
	s_or_b32 s81, s24, 0x12000
	s_nop 4
	s_mov_b32 m0, s23
	s_nop 0
	buffer_load_dwordx4 v210, s[16:19], s81 offen lds
	s_add_i32 s23, s22, 0x12800
	s_or_b32 s81, s24, 0x14000
	s_nop 4
	s_mov_b32 m0, s23
	s_nop 0
	buffer_load_dwordx4 v209, s[16:19], s81 offen lds
	s_add_i32 s23, s22, 0x12c00
	s_or_b32 s81, s24, 0x16000
	s_nop 4
	s_mov_b32 m0, s23
	s_nop 0
	buffer_load_dwordx4 v210, s[16:19], s81 offen lds
	s_add_i32 s23, s22, 0x13000
	s_or_b32 s81, s24, 0x18000
	s_nop 4
	s_mov_b32 m0, s23
	s_nop 0
	buffer_load_dwordx4 v209, s[16:19], s81 offen lds
	s_add_i32 s23, s22, 0x13400
	s_or_b32 s81, s24, 0x1a000
	s_nop 4
	s_mov_b32 m0, s23
	s_nop 0
	buffer_load_dwordx4 v210, s[16:19], s81 offen lds
	s_add_i32 s23, s22, 0x13800
	s_or_b32 s81, s24, 0x1c000
	s_nop 4
	s_mov_b32 m0, s23
	s_nop 0
	buffer_load_dwordx4 v209, s[16:19], s81 offen lds
	s_add_i32 s22, s22, 0x13c00
	s_or_b32 s23, s24, 0x1e000
	s_nop 4
	s_mov_b32 m0, s22
	s_nop 0
	buffer_load_dwordx4 v210, s[16:19], s23 offen lds
	s_add_i32 s16, s33, 0x2000
	s_nop 4
	s_mov_b32 m0, s30
	s_nop 0
	buffer_load_dwordx4 v209, s[4:7], s33 offen lds
	s_add_i32 s17, s33, 0x6000
	s_nop 4
	s_mov_b32 m0, s37
	s_nop 0
	buffer_load_dwordx4 v210, s[4:7], s16 offen lds
	s_add_i32 s16, s33, 0x4000
	s_nop 4
	s_mov_b32 m0, s39
	s_nop 0
	buffer_load_dwordx4 v209, s[4:7], s16 offen lds
	s_mov_b32 s22, s6
	s_nop 4
	s_mov_b32 m0, s41
	s_nop 0
	buffer_load_dwordx4 v210, s[4:7], s17 offen lds
	s_mov_b32 s23, s7
	s_nop 4
	s_mov_b32 m0, s31
	s_nop 0
	buffer_load_dwordx4 v211, s[20:23], s33 offen lds
	s_add_i32 s17, s31, 0x400
	s_add_i32 s19, s33, 0x80
	s_nop 4
	s_mov_b32 m0, s17
	s_nop 0
	buffer_load_dwordx4 v211, s[20:23], s19 offen lds
	s_add_i32 s17, s31, 0x800
	s_nop 4
	s_mov_b32 m0, s17
	s_nop 0
	buffer_load_dwordx4 v211, s[20:23], s16 offen lds
	s_add_i32 s16, s31, 0xc00
	s_add_i32 s17, s33, 0x4080
	s_nop 4
	s_mov_b32 m0, s16
	s_nop 0
	buffer_load_dwordx4 v211, s[20:23], s17 offen lds
	s_add_i32 s16, s33, 0x22000
	s_nop 4
	s_mov_b32 m0, s51
	s_nop 0
	buffer_load_dwordx4 v209, s[4:7], s44 offen lds
	s_nop 0
	s_nop 4
	s_mov_b32 m0, s53
	s_nop 0
	buffer_load_dwordx4 v210, s[4:7], s16 offen lds
	s_add_i32 s16, s33, 0x26000
	s_nop 4
	s_mov_b32 m0, s55
	s_nop 0
	buffer_load_dwordx4 v209, s[4:7], s48 offen lds
	s_nop 0
	s_nop 4
	s_mov_b32 m0, s57
	s_nop 0
	buffer_load_dwordx4 v210, s[4:7], s16 offen lds
	s_waitcnt vmcnt(20)
.LBB2_7:
	v_mov_b32_e32 v64, v215
	v_mov_b32_e32 v65, v216
	v_mov_b32_e32 v66, v217
	v_mov_b32_e32 v67, v218
	s_andn2_b64 vcc, exec, s[0:1]
	ds_read_b128 v[32:35], v64 offset:0
	ds_read_b128 v[36:39], v65 offset:0
	ds_read_b128 v[40:43], v66 offset:0
	ds_read_b128 v[44:47], v67 offset:0
	ds_read_b128 v[48:51], v64 offset:128
	ds_read_b128 v[52:55], v65 offset:128
	ds_read_b128 v[56:59], v66 offset:128
	ds_read_b128 v[60:63], v67 offset:128
	s_nop 0
	s_waitcnt lgkmcnt(0)
	s_nop 0
	v_lshlrev_b32_e32 v68, 16, v32
	v_and_b32_e32 v32, 0xffff0000, v32
	v_lshlrev_b32_e32 v70, 16, v34
	v_and_b32_e32 v34, 0xffff0000, v34
	v_mul_f32_e32 v32, v32, v224
	v_lshlrev_b32_e32 v69, 16, v33
	v_and_b32_e32 v33, 0xffff0000, v33
	v_mul_f32_e32 v34, v34, v224
	v_lshlrev_b32_e32 v71, 16, v35
	v_and_b32_e32 v35, 0xffff0000, v35
	v_mul_f32_e32 v68, v68, v224
	v_mul_f32_e32 v33, v33, v224
	v_mul_f32_e32 v70, v70, v224
	v_mul_f32_e32 v35, v35, v224
	v_mul_f32_e32 v69, v69, v224
	v_mul_f32_e32 v71, v71, v224
	s_nop 0
	v_cvt_pk_bf16_f32 v34, v70, v34
	v_cvt_pk_bf16_f32 v32, v68, v32
	v_cvt_pk_bf16_f32 v35, v71, v35
	v_cvt_pk_bf16_f32 v33, v69, v33
	v_accvgpr_write_b32 a[128], v32
	v_accvgpr_write_b32 a[129], v33
	v_accvgpr_write_b32 a[130], v34
	v_accvgpr_write_b32 a[131], v35
	v_lshlrev_b32_e32 v32, 16, v36
	v_lshlrev_b32_e32 v34, 16, v37
	v_mul_f32_e32 v32, v32, v224
	v_and_b32_e32 v33, 0xffff0000, v36
	v_mul_f32_e32 v34, v34, v224
	v_and_b32_e32 v35, 0xffff0000, v37
	v_lshlrev_b32_e32 v36, 16, v38
	v_and_b32_e32 v37, 0xffff0000, v38
	v_lshlrev_b32_e32 v38, 16, v39
	v_mul_f32_e32 v33, v33, v224
	v_mul_f32_e32 v35, v35, v224
	v_mul_f32_e32 v36, v36, v224
	v_mul_f32_e32 v38, v38, v224
	v_and_b32_e32 v39, 0xffff0000, v39
	v_cvt_pk_bf16_f32 v34, v34, v35
	v_cvt_pk_bf16_f32 v32, v32, v33
	v_mul_f32_e32 v37, v37, v224
	v_mul_f32_e32 v39, v39, v224
	v_and_b32_e32 v33, 0xffff0000, v40
	v_cvt_pk_bf16_f32 v38, v38, v39
	v_cvt_pk_bf16_f32 v36, v36, v37
	v_accvgpr_write_b32 a[132], v32
	v_accvgpr_write_b32 a[133], v34
	v_accvgpr_write_b32 a[134], v36
	v_accvgpr_write_b32 a[135], v38
	v_lshlrev_b32_e32 v32, 16, v40
	v_lshlrev_b32_e32 v34, 16, v41
	v_mul_f32_e32 v32, v32, v224
	v_mul_f32_e32 v34, v34, v224
	v_and_b32_e32 v35, 0xffff0000, v41
	v_lshlrev_b32_e32 v36, 16, v42
	v_lshlrev_b32_e32 v38, 16, v43
	v_mul_f32_e32 v33, v33, v224
	v_mul_f32_e32 v35, v35, v224
	v_mul_f32_e32 v36, v36, v224
	v_and_b32_e32 v37, 0xffff0000, v42
	v_mul_f32_e32 v38, v38, v224
	v_and_b32_e32 v39, 0xffff0000, v43
	v_cvt_pk_bf16_f32 v34, v34, v35
	v_cvt_pk_bf16_f32 v32, v32, v33
	v_mul_f32_e32 v37, v37, v224
	v_mul_f32_e32 v39, v39, v224
	v_and_b32_e32 v33, 0xffff0000, v44
	v_cvt_pk_bf16_f32 v38, v38, v39
	v_cvt_pk_bf16_f32 v36, v36, v37
	v_accvgpr_write_b32 a[136], v32
	v_accvgpr_write_b32 a[137], v34
	v_accvgpr_write_b32 a[138], v36
	v_accvgpr_write_b32 a[139], v38
	v_lshlrev_b32_e32 v32, 16, v44
	v_lshlrev_b32_e32 v34, 16, v45
	v_mul_f32_e32 v32, v32, v224
	v_mul_f32_e32 v34, v34, v224
	v_and_b32_e32 v35, 0xffff0000, v45
	v_lshlrev_b32_e32 v36, 16, v46
	v_lshlrev_b32_e32 v38, 16, v47
	v_mul_f32_e32 v33, v33, v224
	v_mul_f32_e32 v35, v35, v224
	v_mul_f32_e32 v36, v36, v224
	v_and_b32_e32 v37, 0xffff0000, v46
	v_mul_f32_e32 v38, v38, v224
	v_and_b32_e32 v39, 0xffff0000, v47
	v_cvt_pk_bf16_f32 v34, v34, v35
	v_cvt_pk_bf16_f32 v32, v32, v33
	v_mul_f32_e32 v37, v37, v224
	v_mul_f32_e32 v39, v39, v224
	v_and_b32_e32 v33, 0xffff0000, v48
	v_cvt_pk_bf16_f32 v38, v38, v39
	v_cvt_pk_bf16_f32 v36, v36, v37
	v_accvgpr_write_b32 a[140], v32
	v_accvgpr_write_b32 a[141], v34
	v_accvgpr_write_b32 a[142], v36
	v_accvgpr_write_b32 a[143], v38
	v_lshlrev_b32_e32 v32, 16, v48
	v_lshlrev_b32_e32 v34, 16, v49
	v_mul_f32_e32 v32, v32, v224
	v_mul_f32_e32 v34, v34, v224
	v_and_b32_e32 v35, 0xffff0000, v49
	v_lshlrev_b32_e32 v36, 16, v50
	v_lshlrev_b32_e32 v38, 16, v51
	v_mul_f32_e32 v33, v33, v224
	v_mul_f32_e32 v35, v35, v224
	v_mul_f32_e32 v36, v36, v224
	v_and_b32_e32 v37, 0xffff0000, v50
	v_mul_f32_e32 v38, v38, v224
	v_and_b32_e32 v39, 0xffff0000, v51
	v_cvt_pk_bf16_f32 v34, v34, v35
	v_cvt_pk_bf16_f32 v32, v32, v33
	v_mul_f32_e32 v37, v37, v224
	v_mul_f32_e32 v39, v39, v224
	v_and_b32_e32 v33, 0xffff0000, v52
	v_cvt_pk_bf16_f32 v38, v38, v39
	v_cvt_pk_bf16_f32 v36, v36, v37
	v_accvgpr_write_b32 a[144], v32
	v_accvgpr_write_b32 a[145], v34
	v_accvgpr_write_b32 a[146], v36
	v_accvgpr_write_b32 a[147], v38
	v_lshlrev_b32_e32 v32, 16, v52
	v_lshlrev_b32_e32 v34, 16, v53
	v_mul_f32_e32 v32, v32, v224
	v_mul_f32_e32 v34, v34, v224
	v_and_b32_e32 v35, 0xffff0000, v53
	v_lshlrev_b32_e32 v36, 16, v54
	v_lshlrev_b32_e32 v38, 16, v55
	v_mul_f32_e32 v33, v33, v224
	v_mul_f32_e32 v35, v35, v224
	v_mul_f32_e32 v36, v36, v224
	v_and_b32_e32 v37, 0xffff0000, v54
	v_mul_f32_e32 v38, v38, v224
	v_and_b32_e32 v39, 0xffff0000, v55
	v_cvt_pk_bf16_f32 v34, v34, v35
	v_cvt_pk_bf16_f32 v32, v32, v33
	v_mul_f32_e32 v37, v37, v224
	v_mul_f32_e32 v39, v39, v224
	v_and_b32_e32 v33, 0xffff0000, v56
	v_cvt_pk_bf16_f32 v38, v38, v39
	v_cvt_pk_bf16_f32 v36, v36, v37
	v_accvgpr_write_b32 a[148], v32
	v_accvgpr_write_b32 a[149], v34
	v_accvgpr_write_b32 a[150], v36
	v_accvgpr_write_b32 a[151], v38
	v_lshlrev_b32_e32 v32, 16, v56
	v_lshlrev_b32_e32 v34, 16, v57
	v_mul_f32_e32 v32, v32, v224
	v_mul_f32_e32 v34, v34, v224
	v_and_b32_e32 v35, 0xffff0000, v57
	v_lshlrev_b32_e32 v36, 16, v58
	v_lshlrev_b32_e32 v38, 16, v59
	v_mul_f32_e32 v33, v33, v224
	v_mul_f32_e32 v35, v35, v224
	v_mul_f32_e32 v36, v36, v224
	v_and_b32_e32 v37, 0xffff0000, v58
	v_mul_f32_e32 v38, v38, v224
	v_and_b32_e32 v39, 0xffff0000, v59
	v_cvt_pk_bf16_f32 v34, v34, v35
	v_cvt_pk_bf16_f32 v32, v32, v33
	v_mul_f32_e32 v37, v37, v224
	v_mul_f32_e32 v39, v39, v224
	v_and_b32_e32 v33, 0xffff0000, v60
	v_cvt_pk_bf16_f32 v38, v38, v39
	v_cvt_pk_bf16_f32 v36, v36, v37
	v_accvgpr_write_b32 a[152], v32
	v_accvgpr_write_b32 a[153], v34
	v_accvgpr_write_b32 a[154], v36
	v_accvgpr_write_b32 a[155], v38
	v_lshlrev_b32_e32 v32, 16, v60
	v_lshlrev_b32_e32 v34, 16, v61
	v_mul_f32_e32 v32, v32, v224
	v_mul_f32_e32 v34, v34, v224
	v_and_b32_e32 v35, 0xffff0000, v61
	v_lshlrev_b32_e32 v36, 16, v62
	v_lshlrev_b32_e32 v38, 16, v63
	v_mul_f32_e32 v33, v33, v224
	v_mul_f32_e32 v35, v35, v224
	v_mul_f32_e32 v36, v36, v224
	v_and_b32_e32 v37, 0xffff0000, v62
	v_mul_f32_e32 v38, v38, v224
	v_and_b32_e32 v39, 0xffff0000, v63
	v_cvt_pk_bf16_f32 v34, v34, v35
	v_cvt_pk_bf16_f32 v32, v32, v33
	v_mul_f32_e32 v37, v37, v224
	v_mul_f32_e32 v39, v39, v224
	s_nop 0
	v_cvt_pk_bf16_f32 v38, v38, v39
	v_cvt_pk_bf16_f32 v36, v36, v37
	v_accvgpr_write_b32 a[156], v32
	v_accvgpr_write_b32 a[157], v34
	v_accvgpr_write_b32 a[158], v36
	v_accvgpr_write_b32 a[159], v38
	s_waitcnt vmcnt(12)
	ds_read_b128 v[32:35], v64 offset:8192
	ds_read_b128 v[36:39], v65 offset:8192
	ds_read_b128 v[40:43], v66 offset:8192
	ds_read_b128 v[44:47], v67 offset:8192
	ds_read_b128 v[48:51], v64 offset:8320
	ds_read_b128 v[52:55], v65 offset:8320
	ds_read_b128 v[56:59], v66 offset:8320
	ds_read_b128 v[60:63], v67 offset:8320
	s_nop 0
	s_waitcnt lgkmcnt(0)
	s_nop 0
	v_lshlrev_b32_e32 v64, 16, v32
	v_and_b32_e32 v32, 0xffff0000, v32
	v_lshlrev_b32_e32 v65, 16, v33
	v_and_b32_e32 v33, 0xffff0000, v33
	v_lshlrev_b32_e32 v66, 16, v34
	v_and_b32_e32 v34, 0xffff0000, v34
	v_lshlrev_b32_e32 v67, 16, v35
	v_and_b32_e32 v35, 0xffff0000, v35
	v_mul_f32_e32 v32, v32, v224
	v_mul_f32_e32 v33, v33, v224
	v_mul_f32_e32 v34, v34, v224
	v_mul_f32_e32 v35, v35, v224
	v_mul_f32_e32 v64, v64, v224
	v_mul_f32_e32 v65, v65, v224
	v_mul_f32_e32 v66, v66, v224
	v_mul_f32_e32 v67, v67, v224
	s_nop 0
	v_cvt_pk_bf16_f32 v35, v67, v35
	v_cvt_pk_bf16_f32 v34, v66, v34
	v_cvt_pk_bf16_f32 v33, v65, v33
	v_cvt_pk_bf16_f32 v32, v64, v32
	v_accvgpr_write_b32 a[160], v32
	v_accvgpr_write_b32 a[161], v33
	v_accvgpr_write_b32 a[162], v34
	v_accvgpr_write_b32 a[163], v35
	v_lshlrev_b32_e32 v32, 16, v36
	v_and_b32_e32 v33, 0xffff0000, v36
	v_lshlrev_b32_e32 v34, 16, v37
	v_and_b32_e32 v35, 0xffff0000, v37
	v_lshlrev_b32_e32 v36, 16, v38
	v_and_b32_e32 v37, 0xffff0000, v38
	v_lshlrev_b32_e32 v38, 16, v39
	v_mul_f32_e32 v32, v32, v224
	v_mul_f32_e32 v34, v34, v224
	v_mul_f32_e32 v36, v36, v224
	v_mul_f32_e32 v38, v38, v224
	v_and_b32_e32 v39, 0xffff0000, v39
	v_mul_f32_e32 v33, v33, v224
	v_mul_f32_e32 v35, v35, v224
	v_mul_f32_e32 v37, v37, v224
	v_mul_f32_e32 v39, v39, v224
	s_nop 0
	v_cvt_pk_bf16_f32 v38, v38, v39
	v_cvt_pk_bf16_f32 v36, v36, v37
	v_cvt_pk_bf16_f32 v34, v34, v35
	v_cvt_pk_bf16_f32 v32, v32, v33
	v_accvgpr_write_b32 a[164], v32
	v_accvgpr_write_b32 a[165], v34
	v_accvgpr_write_b32 a[166], v36
	v_accvgpr_write_b32 a[167], v38
	v_lshlrev_b32_e32 v32, 16, v40
	v_lshlrev_b32_e32 v34, 16, v41
	v_lshlrev_b32_e32 v36, 16, v42
	v_lshlrev_b32_e32 v38, 16, v43
	v_mul_f32_e32 v32, v32, v224
	v_and_b32_e32 v33, 0xffff0000, v40
	v_mul_f32_e32 v34, v34, v224
	v_and_b32_e32 v35, 0xffff0000, v41
	v_mul_f32_e32 v36, v36, v224
	v_and_b32_e32 v37, 0xffff0000, v42
	v_mul_f32_e32 v38, v38, v224
	v_and_b32_e32 v39, 0xffff0000, v43
	v_mul_f32_e32 v33, v33, v224
	v_mul_f32_e32 v35, v35, v224
	v_mul_f32_e32 v37, v37, v224
	v_mul_f32_e32 v39, v39, v224
	s_nop 0
	v_cvt_pk_bf16_f32 v38, v38, v39
	v_cvt_pk_bf16_f32 v36, v36, v37
	v_cvt_pk_bf16_f32 v34, v34, v35
	v_cvt_pk_bf16_f32 v32, v32, v33
	v_accvgpr_write_b32 a[168], v32
	v_accvgpr_write_b32 a[169], v34
	v_accvgpr_write_b32 a[170], v36
	v_accvgpr_write_b32 a[171], v38
	v_lshlrev_b32_e32 v32, 16, v44
	v_lshlrev_b32_e32 v34, 16, v45
	v_lshlrev_b32_e32 v36, 16, v46
	v_lshlrev_b32_e32 v38, 16, v47
	v_mul_f32_e32 v32, v32, v224
	v_and_b32_e32 v33, 0xffff0000, v44
	v_mul_f32_e32 v34, v34, v224
	v_and_b32_e32 v35, 0xffff0000, v45
	v_mul_f32_e32 v36, v36, v224
	v_and_b32_e32 v37, 0xffff0000, v46
	v_mul_f32_e32 v38, v38, v224
	v_and_b32_e32 v39, 0xffff0000, v47
	v_mul_f32_e32 v33, v33, v224
	v_mul_f32_e32 v35, v35, v224
	v_mul_f32_e32 v37, v37, v224
	v_mul_f32_e32 v39, v39, v224
	s_nop 0
	v_cvt_pk_bf16_f32 v38, v38, v39
	v_cvt_pk_bf16_f32 v36, v36, v37
	v_cvt_pk_bf16_f32 v34, v34, v35
	v_cvt_pk_bf16_f32 v32, v32, v33
	v_accvgpr_write_b32 a[172], v32
	v_accvgpr_write_b32 a[173], v34
	v_accvgpr_write_b32 a[174], v36
	v_accvgpr_write_b32 a[175], v38
	v_lshlrev_b32_e32 v32, 16, v48
	v_lshlrev_b32_e32 v34, 16, v49
	v_lshlrev_b32_e32 v36, 16, v50
	v_lshlrev_b32_e32 v38, 16, v51
	v_mul_f32_e32 v32, v32, v224
	v_and_b32_e32 v33, 0xffff0000, v48
	v_mul_f32_e32 v34, v34, v224
	v_and_b32_e32 v35, 0xffff0000, v49
	v_mul_f32_e32 v36, v36, v224
	v_and_b32_e32 v37, 0xffff0000, v50
	v_mul_f32_e32 v38, v38, v224
	v_and_b32_e32 v39, 0xffff0000, v51
	v_mul_f32_e32 v33, v33, v224
	v_mul_f32_e32 v35, v35, v224
	v_mul_f32_e32 v37, v37, v224
	v_mul_f32_e32 v39, v39, v224
	s_nop 0
	v_cvt_pk_bf16_f32 v38, v38, v39
	v_cvt_pk_bf16_f32 v36, v36, v37
	v_cvt_pk_bf16_f32 v34, v34, v35
	v_cvt_pk_bf16_f32 v32, v32, v33
	v_accvgpr_write_b32 a[176], v32
	v_accvgpr_write_b32 a[177], v34
	v_accvgpr_write_b32 a[178], v36
	v_accvgpr_write_b32 a[179], v38
	v_lshlrev_b32_e32 v32, 16, v52
	v_lshlrev_b32_e32 v34, 16, v53
	v_lshlrev_b32_e32 v36, 16, v54
	v_lshlrev_b32_e32 v38, 16, v55
	v_mul_f32_e32 v32, v32, v224
	v_and_b32_e32 v33, 0xffff0000, v52
	v_mul_f32_e32 v34, v34, v224
	v_and_b32_e32 v35, 0xffff0000, v53
	v_mul_f32_e32 v36, v36, v224
	v_and_b32_e32 v37, 0xffff0000, v54
	v_mul_f32_e32 v38, v38, v224
	v_and_b32_e32 v39, 0xffff0000, v55
	v_mul_f32_e32 v33, v33, v224
	v_mul_f32_e32 v35, v35, v224
	v_mul_f32_e32 v37, v37, v224
	v_mul_f32_e32 v39, v39, v224
	s_nop 0
	v_cvt_pk_bf16_f32 v38, v38, v39
	v_cvt_pk_bf16_f32 v36, v36, v37
	v_cvt_pk_bf16_f32 v34, v34, v35
	v_cvt_pk_bf16_f32 v32, v32, v33
	v_accvgpr_write_b32 a[180], v32
	v_accvgpr_write_b32 a[181], v34
	v_accvgpr_write_b32 a[182], v36
	v_accvgpr_write_b32 a[183], v38
	v_lshlrev_b32_e32 v32, 16, v56
	v_lshlrev_b32_e32 v34, 16, v57
	v_lshlrev_b32_e32 v36, 16, v58
	v_lshlrev_b32_e32 v38, 16, v59
	v_mul_f32_e32 v32, v32, v224
	v_and_b32_e32 v33, 0xffff0000, v56
	v_mul_f32_e32 v34, v34, v224
	v_and_b32_e32 v35, 0xffff0000, v57
	v_mul_f32_e32 v36, v36, v224
	v_and_b32_e32 v37, 0xffff0000, v58
	v_mul_f32_e32 v38, v38, v224
	v_and_b32_e32 v39, 0xffff0000, v59
	v_mul_f32_e32 v33, v33, v224
	v_mul_f32_e32 v35, v35, v224
	v_mul_f32_e32 v37, v37, v224
	v_mul_f32_e32 v39, v39, v224
	s_nop 0
	v_cvt_pk_bf16_f32 v38, v38, v39
	v_cvt_pk_bf16_f32 v36, v36, v37
	v_cvt_pk_bf16_f32 v34, v34, v35
	v_cvt_pk_bf16_f32 v32, v32, v33
	v_accvgpr_write_b32 a[184], v32
	v_accvgpr_write_b32 a[185], v34
	v_accvgpr_write_b32 a[186], v36
	v_accvgpr_write_b32 a[187], v38
	v_lshlrev_b32_e32 v32, 16, v60
	v_lshlrev_b32_e32 v34, 16, v61
	v_lshlrev_b32_e32 v36, 16, v62
	v_lshlrev_b32_e32 v38, 16, v63
	v_mul_f32_e32 v32, v32, v224
	v_and_b32_e32 v33, 0xffff0000, v60
	v_mul_f32_e32 v34, v34, v224
	v_and_b32_e32 v35, 0xffff0000, v61
	v_mul_f32_e32 v36, v36, v224
	v_and_b32_e32 v37, 0xffff0000, v62
	v_mul_f32_e32 v38, v38, v224
	v_and_b32_e32 v39, 0xffff0000, v63
	v_mul_f32_e32 v33, v33, v224
	v_mul_f32_e32 v35, v35, v224
	v_mul_f32_e32 v37, v37, v224
	v_mul_f32_e32 v39, v39, v224
	s_nop 0
	v_cvt_pk_bf16_f32 v38, v38, v39
	v_cvt_pk_bf16_f32 v36, v36, v37
	v_cvt_pk_bf16_f32 v34, v34, v35
	v_cvt_pk_bf16_f32 v32, v32, v33
	v_accvgpr_write_b32 a[188], v32
	v_accvgpr_write_b32 a[189], v34
	v_accvgpr_write_b32 a[190], v36
	v_accvgpr_write_b32 a[191], v38
	s_waitcnt vmcnt(8)
	s_barrier
	s_cbranch_vccnz .LBB2_9
	ds_read_b128 a[192:195], v204 offset:0
	s_nop 0
	ds_read_b128 a[196:199], v205 offset:0
	s_nop 0
	ds_read_b128 a[200:203], v206 offset:0
	s_nop 0
	ds_read_b128 a[204:207], v207 offset:0
	s_nop 0
	ds_read_b128 a[208:211], v204 offset:128
	s_nop 0
	ds_read_b128 a[212:215], v205 offset:128
	s_nop 0
	ds_read_b128 a[216:219], v206 offset:128
	s_nop 0
	ds_read_b128 a[220:223], v207 offset:128
	s_nop 0
	ds_read_b128 a[224:227], v204 offset:8192
	s_nop 0
	ds_read_b128 a[228:231], v205 offset:8192
	s_nop 0
	ds_read_b128 a[232:235], v206 offset:8192
	s_nop 0
	ds_read_b128 a[236:239], v207 offset:8192
	s_nop 0
	ds_read_b128 a[240:243], v204 offset:8320
	s_nop 0
	ds_read_b128 a[244:247], v205 offset:8320
	s_nop 0
	ds_read_b128 a[248:251], v206 offset:8320
	s_nop 0
	ds_read_b128 a[252:255], v207 offset:8320
